# attention row-sum: serial v_add_f32 chain replaced by v_pk_add_f32 on adjacent register pairs (instruction selection)
# baseline (speedup 1.0000x reference)
; DI void finishSM(f32x16& p0, f32x16& p1, float alpha, float& l_reg, bf16x8& pa0, bf16x8& pa1, bf16x8& pa2, bf16x8& pa3) {
; #pragma unroll
;     for (int r = 0; r < 16; ++r) p1[r] = __builtin_amdgcn_exp2f(p1[r]);
;     float ps = 0;
; #pragma unroll
;     for (int r = 0; r < 16; ++r) ps += p0[r];
; #pragma unroll
;     for (int r = 0; r < 16; ++r) ps += p1[r];
;     { auto rr = __builtin_amdgcn_permlane32_swap(__float_as_uint(ps), __float_as_uint(ps), false, false); ps = __uint_as_float(rr[0]) + __uint_as_float(rr[1]); }
;     l_reg = l_reg * alpha + ps;
;     ...
;     AT_PK4(p0, 0, pa0); AT_PK4(p0, 8, pa1); AT_PK4(p1, 0, pa2); AT_PK4(p1, 8, pa3);
;     ...
; }
; DI void qkt(f32x16& p0, f32x16& p1, const char* Ks, const bf16x8* qr, const f32x16& negm, int r32, int hi) {
; #pragma unroll
;     for (int d0 = 0; d0 < 4; ++d0) { const int cb = (d0 * 16 + hi * 8) * 2;
;         const bf16x8 b0 = *reinterpret_cast<const bf16x8*>(Ks + AT_KSWZ(r32, cb));
;         const bf16x8 b1 = *reinterpret_cast<const bf16x8*>(Ks + AT_KSWZ(32 + r32, cb));
;         p0 = __builtin_amdgcn_mfma_f32_32x32x16_bf16(b0, qr[d0], d0 == 0 ? negm : p0, 0, 0, 0);
;         p1 = __builtin_amdgcn_mfma_f32_32x32x16_bf16(b1, qr[d0], d0 == 0 ? negm : p1, 0, 0, 0); }
; }
.LBB4_702:
	s_lshl_b32 s26, s66, 13
	s_add_i32 s26, s26, 0
	v_add_u32_e32 v72, s26, v205
	v_add_u32_e32 v112, s26, v206
	v_add_u32_e32 v180, s26, v207
	s_waitcnt lgkmcnt(1)
	v_mfma_f32_32x32x16_bf16 v[128:143], v[64:67], v[156:159], v[80:95]
	ds_read_b128 v[64:67], v72 offset:49152
	ds_read_b128 v[72:75], v72 offset:53248
	ds_read_b128 v[76:79], v112 offset:49152
	ds_read_b128 v[220:223], v112 offset:53248
	v_exp_f32_e32 v186, v97
	v_exp_f32_e32 v213, v98
	v_exp_f32_e32 v214, v99
	v_exp_f32_e32 v219, v100
	v_exp_f32_e32 v228, v101
	s_waitcnt lgkmcnt(4)
	v_mfma_f32_32x32x16_bf16 v[112:127], v[68:71], v[156:159], v[80:95]
	ds_read_b128 v[68:71], v180 offset:49152
	ds_read_b128 v[224:227], v180 offset:53248
	v_exp_f32_e32 v180, v96
	v_cvt_pk_bf16_f32 v96, v216, v218
	v_cvt_pk_bf16_f32 v97, v179, v217
	v_cvt_pk_bf16_f32 v98, v177, v215
	v_cvt_pk_bf16_f32 v99, v176, v178
	s_waitcnt lgkmcnt(4)
	v_mfma_f32_32x32x16_bf16 v[112:127], v[72:75], v[152:155], v[112:127]
	v_pk_add_f32 v[254:255], v[216:217], 0 op_sel_hi:[1,0]
	v_pk_add_f32 v[254:255], v[176:177], v[254:255]
	v_mfma_f32_32x32x16_bf16 v[128:143], v[64:67], v[152:155], v[128:143]
	v_pk_add_f32 v[254:255], v[178:179], v[254:255]
	v_pk_add_f32 v[254:255], v[174:175], v[254:255]
	v_pk_add_f32 v[254:255], v[172:173], v[254:255]
	s_waitcnt lgkmcnt(3)
	v_mfma_f32_32x32x16_bf16 v[128:143], v[76:79], v[148:151], v[128:143]
	v_pk_add_f32 v[254:255], v[168:169], v[254:255]
	v_pk_add_f32 v[254:255], v[170:171], v[254:255]
	v_add_f32_e32 v254, v180, v254
	v_add_f32_e32 v255, v186, v255
	v_exp_f32_e32 v64, v102
	v_exp_f32_e32 v65, v103
	v_exp_f32_e32 v66, v104
	s_waitcnt lgkmcnt(2)
	v_mfma_f32_32x32x16_bf16 v[112:127], v[220:223], v[148:151], v[112:127]
	v_exp_f32_e32 v67, v105
	v_exp_f32_e32 v105, v106
	v_exp_f32_e32 v106, v107
	v_exp_f32_e32 v107, v108
	v_exp_f32_e32 v72, v109
	v_exp_f32_e32 v73, v110
	v_exp_f32_e32 v74, v111
	s_waitcnt lgkmcnt(1)
	v_mfma_f32_32x32x16_bf16 v[128:143], v[68:71], v[144:147], v[128:143]
	v_add_f32_e32 v254, v213, v254
	v_pk_add_f32 v[254:255], v[214:215], v[254:255]
	v_pk_add_f32 v[254:255], v[218:219], v[254:255]
	v_add_f32_e32 v255, v228, v255
	v_pk_add_f32 v[254:255], v[64:65], v[254:255]
	v_pk_add_f32 v[254:255], v[66:67], v[254:255]
	s_waitcnt lgkmcnt(0)
	v_mfma_f32_32x32x16_bf16 v[112:127], v[224:227], v[144:147], v[112:127]
	v_add_f32_e32 v254, v105, v254
	v_pk_add_f32 v[254:255], v[106:107], v[254:255]
	v_pk_add_f32 v[254:255], v[72:73], v[254:255]
	v_add_f32_e32 v255, v74, v255
	v_add_f32_e32 v183, v254, v255
	v_mov_b32_e32 v212, v183
	v_cvt_pk_bf16_f32 v108, v173, v175
	v_cvt_pk_bf16_f32 v109, v171, v174
	v_cvt_pk_bf16_f32 v110, v169, v172
	v_cvt_pk_bf16_f32 v111, v168, v170
	v_cvt_pk_bf16_f32 v100, v180, v186
	v_cvt_pk_bf16_f32 v101, v213, v214
	v_cvt_pk_bf16_f32 v102, v219, v228
	v_cvt_pk_bf16_f32 v103, v64, v65
	v_cvt_pk_bf16_f32 v104, v66, v67
	v_cvt_pk_bf16_f32 v105, v105, v106
	v_cvt_pk_bf16_f32 v106, v107, v72
	v_cvt_pk_bf16_f32 v107, v73, v74
	s_nop 1
	v_permlane32_swap_b32_e32 v183, v212
	v_permlane32_swap_b32_e32 v96, v98
	v_permlane32_swap_b32_e32 v97, v99
	v_permlane32_swap_b32_e32 v108, v110
	v_permlane32_swap_b32_e32 v109, v111
	v_permlane32_swap_b32_e32 v100, v102
	v_permlane32_swap_b32_e32 v101, v103
	v_permlane32_swap_b32_e32 v104, v106
	v_permlane32_swap_b32_e32 v105, v107
	s_add_u32 s74, s46, s28
	s_addc_u32 s75, s47, s29
	s_add_u32 s78, s74, 0x23808000
	s_addc_u32 s79, s75, 0
	s_add_u32 s80, s74, 0x2380a000
	s_addc_u32 s81, s75, 0
	s_add_u32 s76, s46, s30
	s_addc_u32 s77, s47, s31
	s_add_u32 s82, s76, 0x21804000
	s_addc_u32 s83, s77, 0
	v_mov_b32_e32 v64, v198
	v_mov_b32_e32 v65, v197
	global_load_dwordx4 v[176:179], v65, s[78:79]
	global_load_dwordx4 v[172:175], v65, s[80:81]
	global_load_dwordx4 v[168:171], v64, s[82:83]
	s_andn2_b64 vcc, exec, s[2:3]
	s_cbranch_vccnz .LBB4_704
	s_mov_b64 s[2:3], s[8:9]
	v_mov_b32_e32 v64, v189
	global_store_dwordx2 v64, v[184:185], s[2:3] nt

; DI void finishSM(f32x16& p0, f32x16& p1, float alpha, float& l_reg, bf16x8& pa0, bf16x8& pa1, bf16x8& pa2, bf16x8& pa3) {
; #pragma unroll
;     for (int r = 0; r < 16; ++r) p1[r] = __builtin_amdgcn_exp2f(p1[r]);
;     float ps = 0;
; #pragma unroll
;     for (int r = 0; r < 16; ++r) ps += p0[r];
; #pragma unroll
;     for (int r = 0; r < 16; ++r) ps += p1[r];
;     { auto rr = __builtin_amdgcn_permlane32_swap(__float_as_uint(ps), __float_as_uint(ps), false, false); ps = __uint_as_float(rr[0]) + __uint_as_float(rr[1]); }
;     l_reg = l_reg * alpha + ps;
;     ...
;     AT_PK4(p0, 0, pa0); AT_PK4(p0, 8, pa1); AT_PK4(p1, 0, pa2); AT_PK4(p1, 8, pa3);
;     ...
; }
; DI void qkt(f32x16& p0, f32x16& p1, const char* Ks, const bf16x8* qr, const f32x16& negm, int r32, int hi) {
; #pragma unroll
;     for (int d0 = 0; d0 < 4; ++d0) { const int cb = (d0 * 16 + hi * 8) * 2;
;         const bf16x8 b0 = *reinterpret_cast<const bf16x8*>(Ks + AT_KSWZ(r32, cb));
;         const bf16x8 b1 = *reinterpret_cast<const bf16x8*>(Ks + AT_KSWZ(32 + r32, cb));
;         p0 = __builtin_amdgcn_mfma_f32_32x32x16_bf16(b0, qr[d0], d0 == 0 ? negm : p0, 0, 0, 0);
;         p1 = __builtin_amdgcn_mfma_f32_32x32x16_bf16(b1, qr[d0], d0 == 0 ? negm : p1, 0, 0, 0); }
; }
.LBB4_723:
	v_exp_f32_e32 v186, v128
	v_exp_f32_e32 v230, v129
	v_exp_f32_e32 v231, v130
	v_exp_f32_e32 v232, v131
	v_exp_f32_e32 v233, v132
	v_exp_f32_e32 v234, v133
	v_exp_f32_e32 v235, v134
	v_exp_f32_e32 v236, v135
	v_exp_f32_e32 v237, v136
	v_exp_f32_e32 v238, v137
	v_exp_f32_e32 v239, v138
	v_exp_f32_e32 v240, v139
	v_exp_f32_e32 v241, v140
	v_exp_f32_e32 v242, v141
	v_exp_f32_e32 v243, v142
	v_exp_f32_e32 v244, v143
	v_add_u32_e32 v101, s78, v205
	v_add_u32_e32 v102, s78, v206
	v_add_u32_e32 v103, s78, v207
	ds_read_b128 v[172:175], v101 offset:49152
	ds_read_b128 v[176:179], v101 offset:53248
	ds_read_b128 v[214:217], v102 offset:49152
	ds_read_b128 v[218:221], v102 offset:53248
	ds_read_b128 v[222:225], v103 offset:49152
	ds_read_b128 v[226:229], v103 offset:53248
	v_exp_f32_e32 v112, v112
	v_exp_f32_e32 v113, v113
	v_exp_f32_e32 v114, v114
	s_waitcnt lgkmcnt(7)
	v_mfma_f32_32x32x16_bf16 v[128:143], v[96:99], v[156:159], v[80:95]
	v_exp_f32_e32 v115, v115
	v_exp_f32_e32 v116, v116
	v_exp_f32_e32 v117, v117
	v_exp_f32_e32 v118, v118
	v_exp_f32_e32 v119, v119
	s_waitcnt lgkmcnt(6)
	v_mfma_f32_32x32x16_bf16 v[96:111], v[168:171], v[156:159], v[80:95]
	v_exp_f32_e32 v168, v120
	v_mov_b32_e32 v254, v186
	v_mov_b32_e32 v255, 0
	v_pk_add_f32 v[254:255], v[230:231], v[254:255]
	v_pk_add_f32 v[254:255], v[232:233], v[254:255]
	v_pk_add_f32 v[254:255], v[234:235], v[254:255]
	v_pk_add_f32 v[254:255], v[236:237], v[254:255]
	s_waitcnt lgkmcnt(5)
	v_mfma_f32_32x32x16_bf16 v[128:143], v[172:175], v[152:155], v[128:143]
	v_pk_add_f32 v[254:255], v[238:239], v[254:255]
	v_pk_add_f32 v[254:255], v[240:241], v[254:255]
	v_pk_add_f32 v[254:255], v[242:243], v[254:255]
	v_add_f32_e32 v255, v244, v255
	s_waitcnt lgkmcnt(4)
	v_mfma_f32_32x32x16_bf16 v[96:111], v[176:179], v[152:155], v[96:111]
	v_pk_add_f32 v[254:255], v[112:113], v[254:255]
	v_pk_add_f32 v[254:255], v[114:115], v[254:255]
	v_exp_f32_e32 v169, v121
	v_pk_add_f32 v[254:255], v[116:117], v[254:255]
	v_exp_f32_e32 v170, v122
	s_waitcnt lgkmcnt(3)
	v_mfma_f32_32x32x16_bf16 v[128:143], v[214:217], v[148:151], v[128:143]
	v_exp_f32_e32 v171, v123
	v_pk_add_f32 v[254:255], v[118:119], v[254:255]
	v_exp_f32_e32 v172, v124
	v_exp_f32_e32 v173, v125
	v_pk_add_f32 v[254:255], v[168:169], v[254:255]
	s_waitcnt lgkmcnt(2)
	v_mfma_f32_32x32x16_bf16 v[96:111], v[218:221], v[148:151], v[96:111]
	v_exp_f32_e32 v174, v126
	v_exp_f32_e32 v175, v127
	v_pk_add_f32 v[254:255], v[170:171], v[254:255]
	v_pk_add_f32 v[254:255], v[172:173], v[254:255]
	s_waitcnt lgkmcnt(1)
	v_mfma_f32_32x32x16_bf16 v[128:143], v[222:225], v[144:147], v[128:143]
	v_pk_add_f32 v[254:255], v[174:175], v[254:255]
	v_add_f32_e32 v213, v254, v255
	v_mov_b32_e32 v214, v213
	v_cvt_pk_bf16_f32 v120, v186, v230
	v_cvt_pk_bf16_f32 v121, v231, v232
	v_cvt_pk_bf16_f32 v122, v233, v234
	v_cvt_pk_bf16_f32 v123, v235, v236
	v_cvt_pk_bf16_f32 v124, v237, v238
	s_waitcnt lgkmcnt(0)
	v_mfma_f32_32x32x16_bf16 v[96:111], v[226:229], v[144:147], v[96:111]
	v_cvt_pk_bf16_f32 v125, v239, v240
	v_cvt_pk_bf16_f32 v126, v241, v242
	v_cvt_pk_bf16_f32 v127, v243, v244
	v_cvt_pk_bf16_f32 v112, v112, v113
	v_cvt_pk_bf16_f32 v113, v114, v115
	v_cvt_pk_bf16_f32 v114, v116, v117
	v_cvt_pk_bf16_f32 v115, v118, v119
	v_cvt_pk_bf16_f32 v116, v168, v169
	v_cvt_pk_bf16_f32 v117, v170, v171
	v_cvt_pk_bf16_f32 v118, v172, v173
	v_cvt_pk_bf16_f32 v119, v174, v175
	v_permlane32_swap_b32_e32 v213, v214
	v_permlane32_swap_b32_e32 v120, v122
	v_permlane32_swap_b32_e32 v121, v123
	v_permlane32_swap_b32_e32 v124, v126
	v_permlane32_swap_b32_e32 v125, v127
	v_permlane32_swap_b32_e32 v112, v114
	v_permlane32_swap_b32_e32 v113, v115
	v_permlane32_swap_b32_e32 v116, v118
	v_permlane32_swap_b32_e32 v117, v119
	s_add_u32 s78, s74, 0x2380c000
	s_addc_u32 s79, s75, 0
	s_add_u32 s74, s74, 0x2380e000
	s_addc_u32 s75, s75, 0
	s_add_u32 s76, s76, 0x21806000
	s_addc_u32 s77, s77, 0
	v_mov_b32_e32 v168, v198
	v_mov_b32_e32 v169, v197
	global_load_dwordx4 v[176:179], v169, s[78:79]
	global_load_dwordx4 v[172:175], v169, s[74:75]
	s_nop 0
	global_load_dwordx4 v[168:171], v168, s[76:77]
	s_and_b64 vcc, exec, s[2:3]
	s_cbranch_vccnz .LBB4_725
	s_mov_b64 s[2:3], s[8:9]
	v_mov_b32_e32 v186, v189
	global_store_dwordx2 v186, v[184:185], s[2:3] nt

; DI void finishSM(f32x16& p0, f32x16& p1, float alpha, float& l_reg, bf16x8& pa0, bf16x8& pa1, bf16x8& pa2, bf16x8& pa3) {
; #pragma unroll
;     for (int r = 0; r < 16; ++r) p1[r] = __builtin_amdgcn_exp2f(p1[r]);
;     float ps = 0;
; #pragma unroll
;     for (int r = 0; r < 16; ++r) ps += p0[r];
; #pragma unroll
;     for (int r = 0; r < 16; ++r) ps += p1[r];
;     { auto rr = __builtin_amdgcn_permlane32_swap(__float_as_uint(ps), __float_as_uint(ps), false, false); ps = __uint_as_float(rr[0]) + __uint_as_float(rr[1]); }
;     l_reg = l_reg * alpha + ps;
;     ...
;     AT_PK4(p0, 0, pa0); AT_PK4(p0, 8, pa1); AT_PK4(p1, 0, pa2); AT_PK4(p1, 8, pa3);
;     ...
; }
; DI void qkt(f32x16& p0, f32x16& p1, const char* Ks, const bf16x8* qr, const f32x16& negm, int r32, int hi) {
; #pragma unroll
;     for (int d0 = 0; d0 < 4; ++d0) { const int cb = (d0 * 16 + hi * 8) * 2;
;         const bf16x8 b0 = *reinterpret_cast<const bf16x8*>(Ks + AT_KSWZ(r32, cb));
;         const bf16x8 b1 = *reinterpret_cast<const bf16x8*>(Ks + AT_KSWZ(32 + r32, cb));
;         p0 = __builtin_amdgcn_mfma_f32_32x32x16_bf16(b0, qr[d0], d0 == 0 ? negm : p0, 0, 0, 0);
;         p1 = __builtin_amdgcn_mfma_f32_32x32x16_bf16(b1, qr[d0], d0 == 0 ? negm : p1, 0, 0, 0); }
; }
.LBB4_775:
	s_lshl_b32 s20, s30, 13
	s_add_i32 s20, s20, 0
	v_add_u32_e32 v72, s20, v208
	v_add_u32_e32 v112, s20, v209
	v_add_u32_e32 v180, s20, v210
	s_waitcnt lgkmcnt(1)
	v_mfma_f32_32x32x16_bf16 v[128:143], v[64:67], v[156:159], v[80:95]
	ds_read_b128 v[64:67], v72 offset:49152
	ds_read_b128 v[72:75], v72 offset:53248
	ds_read_b128 v[76:79], v112 offset:49152
	ds_read_b128 v[224:227], v112 offset:53248
	v_exp_f32_e32 v182, v97
	v_exp_f32_e32 v217, v98
	v_exp_f32_e32 v218, v99
	v_exp_f32_e32 v223, v100
	v_exp_f32_e32 v232, v101
	s_waitcnt lgkmcnt(4)
	v_mfma_f32_32x32x16_bf16 v[112:127], v[68:71], v[156:159], v[80:95]
	ds_read_b128 v[68:71], v180 offset:49152
	ds_read_b128 v[228:231], v180 offset:53248
	v_exp_f32_e32 v180, v96
	v_cvt_pk_bf16_f32 v96, v220, v222
	v_cvt_pk_bf16_f32 v97, v179, v221
	v_cvt_pk_bf16_f32 v98, v177, v219
	v_cvt_pk_bf16_f32 v99, v176, v178
	s_waitcnt lgkmcnt(4)
	v_mfma_f32_32x32x16_bf16 v[112:127], v[72:75], v[152:155], v[112:127]
	v_pk_add_f32 v[254:255], v[220:221], 0 op_sel_hi:[1,0]
	v_pk_add_f32 v[254:255], v[176:177], v[254:255]
	v_mfma_f32_32x32x16_bf16 v[128:143], v[64:67], v[152:155], v[128:143]
	v_pk_add_f32 v[254:255], v[178:179], v[254:255]
	v_pk_add_f32 v[254:255], v[174:175], v[254:255]
	v_pk_add_f32 v[254:255], v[172:173], v[254:255]
	s_waitcnt lgkmcnt(3)
	v_mfma_f32_32x32x16_bf16 v[128:143], v[76:79], v[148:151], v[128:143]
	v_pk_add_f32 v[254:255], v[168:169], v[254:255]
	v_pk_add_f32 v[254:255], v[170:171], v[254:255]
	v_add_f32_e32 v254, v180, v254
	v_add_f32_e32 v255, v182, v255
	v_exp_f32_e32 v64, v102
	v_exp_f32_e32 v65, v103
	v_exp_f32_e32 v66, v104
	s_waitcnt lgkmcnt(2)
	v_mfma_f32_32x32x16_bf16 v[112:127], v[224:227], v[148:151], v[112:127]
	v_exp_f32_e32 v67, v105
	v_exp_f32_e32 v105, v106
	v_exp_f32_e32 v106, v107
	v_exp_f32_e32 v107, v108
	v_exp_f32_e32 v72, v109
	v_exp_f32_e32 v73, v110
	v_exp_f32_e32 v74, v111
	s_waitcnt lgkmcnt(1)
	v_mfma_f32_32x32x16_bf16 v[128:143], v[68:71], v[144:147], v[128:143]
	v_add_f32_e32 v254, v217, v254
	v_pk_add_f32 v[254:255], v[218:219], v[254:255]
	v_pk_add_f32 v[254:255], v[222:223], v[254:255]
	v_add_f32_e32 v255, v232, v255
	v_pk_add_f32 v[254:255], v[64:65], v[254:255]
	v_pk_add_f32 v[254:255], v[66:67], v[254:255]
	s_waitcnt lgkmcnt(0)
	v_mfma_f32_32x32x16_bf16 v[112:127], v[228:231], v[144:147], v[112:127]
	v_add_f32_e32 v254, v105, v254
	v_pk_add_f32 v[254:255], v[106:107], v[254:255]
	v_pk_add_f32 v[254:255], v[72:73], v[254:255]
	v_add_f32_e32 v255, v74, v255
	v_add_f32_e32 v215, v254, v255
	v_mov_b32_e32 v216, v215
	v_cvt_pk_bf16_f32 v108, v173, v175
	v_cvt_pk_bf16_f32 v109, v171, v174
	v_cvt_pk_bf16_f32 v110, v169, v172
	v_cvt_pk_bf16_f32 v111, v168, v170
	v_cvt_pk_bf16_f32 v100, v180, v182
	v_cvt_pk_bf16_f32 v101, v217, v218
	v_cvt_pk_bf16_f32 v102, v223, v232
	v_cvt_pk_bf16_f32 v103, v64, v65
	v_cvt_pk_bf16_f32 v104, v66, v67
	v_cvt_pk_bf16_f32 v105, v105, v106
	v_cvt_pk_bf16_f32 v106, v107, v72
	v_cvt_pk_bf16_f32 v107, v73, v74
	s_nop 1
	v_permlane32_swap_b32_e32 v215, v216
	v_permlane32_swap_b32_e32 v96, v98
	v_permlane32_swap_b32_e32 v97, v99
	v_permlane32_swap_b32_e32 v108, v110
	v_permlane32_swap_b32_e32 v109, v111
	v_permlane32_swap_b32_e32 v100, v102
	v_permlane32_swap_b32_e32 v101, v103
	v_permlane32_swap_b32_e32 v104, v106
	v_permlane32_swap_b32_e32 v105, v107
	s_add_u32 s34, s46, s16
	s_addc_u32 s35, s47, s17
	s_add_u32 s24, s34, 0x23808000
	s_addc_u32 s25, s35, 0
	s_add_u32 s66, s34, 0x2380a000
	s_addc_u32 s67, s35, 0
	s_add_u32 s37, s46, s18
	s_addc_u32 s64, s47, s19
	s_add_u32 s74, s37, 0x21884000
	s_addc_u32 s75, s64, 0
	v_mov_b32_e32 v64, v200
	v_mov_b32_e32 v65, v201
	global_load_dwordx4 v[176:179], v64, s[24:25]
	global_load_dwordx4 v[172:175], v64, s[66:67]
	global_load_dwordx4 v[168:171], v65, s[74:75]
	s_andn2_b64 vcc, exec, s[2:3]
	s_cbranch_vccnz .LBB4_777
	s_mov_b64 s[2:3], s[8:9]
	v_mov_b32_e32 v64, v193
	global_store_dwordx2 v64, v[184:185], s[2:3] nt

; DI void finishSM(f32x16& p0, f32x16& p1, float alpha, float& l_reg, bf16x8& pa0, bf16x8& pa1, bf16x8& pa2, bf16x8& pa3) {
; #pragma unroll
;     for (int r = 0; r < 16; ++r) p1[r] = __builtin_amdgcn_exp2f(p1[r]);
;     float ps = 0;
; #pragma unroll
;     for (int r = 0; r < 16; ++r) ps += p0[r];
; #pragma unroll
;     for (int r = 0; r < 16; ++r) ps += p1[r];
;     { auto rr = __builtin_amdgcn_permlane32_swap(__float_as_uint(ps), __float_as_uint(ps), false, false); ps = __uint_as_float(rr[0]) + __uint_as_float(rr[1]); }
;     l_reg = l_reg * alpha + ps;
;     ...
;     AT_PK4(p0, 0, pa0); AT_PK4(p0, 8, pa1); AT_PK4(p1, 0, pa2); AT_PK4(p1, 8, pa3);
;     ...
; }
; DI void qkt(f32x16& p0, f32x16& p1, const char* Ks, const bf16x8* qr, const f32x16& negm, int r32, int hi) {
; #pragma unroll
;     for (int d0 = 0; d0 < 4; ++d0) { const int cb = (d0 * 16 + hi * 8) * 2;
;         const bf16x8 b0 = *reinterpret_cast<const bf16x8*>(Ks + AT_KSWZ(r32, cb));
;         const bf16x8 b1 = *reinterpret_cast<const bf16x8*>(Ks + AT_KSWZ(32 + r32, cb));
;         p0 = __builtin_amdgcn_mfma_f32_32x32x16_bf16(b0, qr[d0], d0 == 0 ? negm : p0, 0, 0, 0);
;         p1 = __builtin_amdgcn_mfma_f32_32x32x16_bf16(b1, qr[d0], d0 == 0 ? negm : p1, 0, 0, 0); }
; }
.LBB4_796:
	v_exp_f32_e32 v182, v128
	v_exp_f32_e32 v234, v129
	v_exp_f32_e32 v235, v130
	v_exp_f32_e32 v236, v131
	v_exp_f32_e32 v237, v132
	v_exp_f32_e32 v238, v133
	v_exp_f32_e32 v239, v134
	v_exp_f32_e32 v240, v135
	v_exp_f32_e32 v241, v136
	v_exp_f32_e32 v242, v137
	v_exp_f32_e32 v243, v138
	v_exp_f32_e32 v244, v139
	v_exp_f32_e32 v245, v140
	v_exp_f32_e32 v246, v141
	v_exp_f32_e32 v247, v142
	v_exp_f32_e32 v248, v143
	v_add_u32_e32 v101, s65, v208
	v_add_u32_e32 v102, s65, v209
	v_add_u32_e32 v103, s65, v210
	ds_read_b128 v[172:175], v101 offset:49152
	ds_read_b128 v[176:179], v101 offset:53248
	ds_read_b128 v[218:221], v102 offset:49152
	ds_read_b128 v[222:225], v102 offset:53248
	ds_read_b128 v[226:229], v103 offset:49152
	ds_read_b128 v[230:233], v103 offset:53248
	v_exp_f32_e32 v112, v112
	v_exp_f32_e32 v113, v113
	v_exp_f32_e32 v114, v114
	s_waitcnt lgkmcnt(7)
	v_mfma_f32_32x32x16_bf16 v[128:143], v[96:99], v[156:159], v[80:95]
	v_exp_f32_e32 v115, v115
	v_exp_f32_e32 v116, v116
	v_exp_f32_e32 v117, v117
	v_exp_f32_e32 v118, v118
	v_exp_f32_e32 v119, v119
	s_waitcnt lgkmcnt(6)
	v_mfma_f32_32x32x16_bf16 v[96:111], v[168:171], v[156:159], v[80:95]
	v_exp_f32_e32 v168, v120
	v_mov_b32_e32 v254, v182
	v_mov_b32_e32 v255, 0
	v_pk_add_f32 v[254:255], v[234:235], v[254:255]
	v_pk_add_f32 v[254:255], v[236:237], v[254:255]
	v_pk_add_f32 v[254:255], v[238:239], v[254:255]
	v_pk_add_f32 v[254:255], v[240:241], v[254:255]
	s_waitcnt lgkmcnt(5)
	v_mfma_f32_32x32x16_bf16 v[128:143], v[172:175], v[152:155], v[128:143]
	v_pk_add_f32 v[254:255], v[242:243], v[254:255]
	v_pk_add_f32 v[254:255], v[244:245], v[254:255]
	v_pk_add_f32 v[254:255], v[246:247], v[254:255]
	v_add_f32_e32 v255, v248, v255
	s_waitcnt lgkmcnt(4)
	v_mfma_f32_32x32x16_bf16 v[96:111], v[176:179], v[152:155], v[96:111]
	v_pk_add_f32 v[254:255], v[112:113], v[254:255]
	v_pk_add_f32 v[254:255], v[114:115], v[254:255]
	v_exp_f32_e32 v169, v121
	v_pk_add_f32 v[254:255], v[116:117], v[254:255]
	v_exp_f32_e32 v170, v122
	s_waitcnt lgkmcnt(3)
	v_mfma_f32_32x32x16_bf16 v[128:143], v[218:221], v[148:151], v[128:143]
	v_exp_f32_e32 v171, v123
	v_pk_add_f32 v[254:255], v[118:119], v[254:255]
	v_exp_f32_e32 v172, v124
	v_exp_f32_e32 v173, v125
	v_pk_add_f32 v[254:255], v[168:169], v[254:255]
	s_waitcnt lgkmcnt(2)
	v_mfma_f32_32x32x16_bf16 v[96:111], v[222:225], v[148:151], v[96:111]
	v_exp_f32_e32 v174, v126
	v_exp_f32_e32 v175, v127
	v_pk_add_f32 v[254:255], v[170:171], v[254:255]
	v_pk_add_f32 v[254:255], v[172:173], v[254:255]
	s_waitcnt lgkmcnt(1)
	v_mfma_f32_32x32x16_bf16 v[128:143], v[226:229], v[144:147], v[128:143]
	v_pk_add_f32 v[254:255], v[174:175], v[254:255]
	v_add_f32_e32 v217, v254, v255
	v_mov_b32_e32 v218, v217
	v_cvt_pk_bf16_f32 v120, v182, v234
	v_cvt_pk_bf16_f32 v121, v235, v236
	v_cvt_pk_bf16_f32 v122, v237, v238
	v_cvt_pk_bf16_f32 v123, v239, v240
	v_cvt_pk_bf16_f32 v124, v241, v242
	s_waitcnt lgkmcnt(0)
	v_mfma_f32_32x32x16_bf16 v[96:111], v[230:233], v[144:147], v[96:111]
	v_cvt_pk_bf16_f32 v125, v243, v244
	v_cvt_pk_bf16_f32 v126, v245, v246
	v_cvt_pk_bf16_f32 v127, v247, v248
	v_cvt_pk_bf16_f32 v112, v112, v113
	v_cvt_pk_bf16_f32 v113, v114, v115
	v_cvt_pk_bf16_f32 v114, v116, v117
	v_cvt_pk_bf16_f32 v115, v118, v119
	v_cvt_pk_bf16_f32 v116, v168, v169
	v_cvt_pk_bf16_f32 v117, v170, v171
	v_cvt_pk_bf16_f32 v118, v172, v173
	v_cvt_pk_bf16_f32 v119, v174, v175
	v_permlane32_swap_b32_e32 v217, v218
	v_permlane32_swap_b32_e32 v120, v122
	v_permlane32_swap_b32_e32 v121, v123
	v_permlane32_swap_b32_e32 v124, v126
	v_permlane32_swap_b32_e32 v125, v127
	v_permlane32_swap_b32_e32 v112, v114
	v_permlane32_swap_b32_e32 v113, v115
	v_permlane32_swap_b32_e32 v116, v118
	v_permlane32_swap_b32_e32 v117, v119
	s_add_u32 s24, s34, 0x2380c000
	s_addc_u32 s25, s35, 0
	s_add_u32 s34, s34, 0x2380e000
	s_addc_u32 s35, s35, 0
	s_add_u32 s66, s37, 0x21886000
	s_addc_u32 s67, s64, 0
	v_mov_b32_e32 v168, v200
	v_mov_b32_e32 v169, v201
	global_load_dwordx4 v[176:179], v168, s[24:25]
	global_load_dwordx4 v[172:175], v168, s[34:35]
	s_nop 0
	global_load_dwordx4 v[168:171], v169, s[66:67]
	s_and_b64 vcc, exec, s[2:3]
	s_cbranch_vccnz .LBB4_798
	v_mov_b32_e32 v182, v193
	s_mov_b64 s[2:3], s[8:9]
	global_store_dwordx2 v182, v[184:185], s[2:3] nt

; DI void finishSM(f32x16& p0, f32x16& p1, float alpha, float& l_reg, bf16x8& pa0, bf16x8& pa1, bf16x8& pa2, bf16x8& pa3) {
; #pragma unroll
;     for (int r = 0; r < 16; ++r) p1[r] = __builtin_amdgcn_exp2f(p1[r]);
;     float ps = 0;
; #pragma unroll
;     for (int r = 0; r < 16; ++r) ps += p0[r];
; #pragma unroll
;     for (int r = 0; r < 16; ++r) ps += p1[r];
;     { auto rr = __builtin_amdgcn_permlane32_swap(__float_as_uint(ps), __float_as_uint(ps), false, false); ps = __uint_as_float(rr[0]) + __uint_as_float(rr[1]); }
;     l_reg = l_reg * alpha + ps;
;     ...
;     AT_PK4(p0, 0, pa0); AT_PK4(p0, 8, pa1); AT_PK4(p1, 0, pa2); AT_PK4(p1, 8, pa3);
;     ...
; }
; DI void qkt(f32x16& p0, f32x16& p1, const char* Ks, const bf16x8* qr, const f32x16& negm, int r32, int hi) {
; #pragma unroll
;     for (int d0 = 0; d0 < 4; ++d0) { const int cb = (d0 * 16 + hi * 8) * 2;
;         const bf16x8 b0 = *reinterpret_cast<const bf16x8*>(Ks + AT_KSWZ(r32, cb));
;         const bf16x8 b1 = *reinterpret_cast<const bf16x8*>(Ks + AT_KSWZ(32 + r32, cb));
;         p0 = __builtin_amdgcn_mfma_f32_32x32x16_bf16(b0, qr[d0], d0 == 0 ? negm : p0, 0, 0, 0);
;         p1 = __builtin_amdgcn_mfma_f32_32x32x16_bf16(b1, qr[d0], d0 == 0 ? negm : p1, 0, 0, 0); }
; }
.LBB4_849:
	s_lshl_b32 s26, s64, 13
	s_add_i32 s26, s26, 0
	v_add_u32_e32 v72, s26, v204
	v_add_u32_e32 v112, s26, v205
	v_add_u32_e32 v180, s26, v206
	s_waitcnt lgkmcnt(1)
	v_mfma_f32_32x32x16_bf16 v[128:143], v[64:67], v[156:159], v[80:95]
	ds_read_b128 v[64:67], v72 offset:49152
	ds_read_b128 v[72:75], v72 offset:53248
	ds_read_b128 v[76:79], v112 offset:49152
	ds_read_b128 v[220:223], v112 offset:53248
	v_exp_f32_e32 v182, v97
	v_exp_f32_e32 v213, v98
	v_exp_f32_e32 v214, v99
	v_exp_f32_e32 v219, v100
	v_exp_f32_e32 v228, v101
	s_waitcnt lgkmcnt(4)
	v_mfma_f32_32x32x16_bf16 v[112:127], v[68:71], v[156:159], v[80:95]
	ds_read_b128 v[68:71], v180 offset:49152
	ds_read_b128 v[224:227], v180 offset:53248
	v_exp_f32_e32 v180, v96
	v_cvt_pk_bf16_f32 v96, v216, v218
	v_cvt_pk_bf16_f32 v97, v179, v217
	v_cvt_pk_bf16_f32 v98, v177, v215
	v_cvt_pk_bf16_f32 v99, v176, v178
	s_waitcnt lgkmcnt(4)
	v_mfma_f32_32x32x16_bf16 v[112:127], v[72:75], v[152:155], v[112:127]
	v_pk_add_f32 v[254:255], v[216:217], 0 op_sel_hi:[1,0]
	v_pk_add_f32 v[254:255], v[176:177], v[254:255]
	v_mfma_f32_32x32x16_bf16 v[128:143], v[64:67], v[152:155], v[128:143]
	v_pk_add_f32 v[254:255], v[178:179], v[254:255]
	v_pk_add_f32 v[254:255], v[174:175], v[254:255]
	v_pk_add_f32 v[254:255], v[172:173], v[254:255]
	s_waitcnt lgkmcnt(3)
	v_mfma_f32_32x32x16_bf16 v[128:143], v[76:79], v[148:151], v[128:143]
	v_pk_add_f32 v[254:255], v[168:169], v[254:255]
	v_pk_add_f32 v[254:255], v[170:171], v[254:255]
	v_add_f32_e32 v254, v180, v254
	v_add_f32_e32 v255, v182, v255
	v_exp_f32_e32 v64, v102
	v_exp_f32_e32 v65, v103
	v_exp_f32_e32 v66, v104
	s_waitcnt lgkmcnt(2)
	v_mfma_f32_32x32x16_bf16 v[112:127], v[220:223], v[148:151], v[112:127]
	v_exp_f32_e32 v67, v105
	v_exp_f32_e32 v105, v106
	v_exp_f32_e32 v106, v107
	v_exp_f32_e32 v107, v108
	v_exp_f32_e32 v72, v109
	v_exp_f32_e32 v73, v110
	v_exp_f32_e32 v74, v111
	s_waitcnt lgkmcnt(1)
	v_mfma_f32_32x32x16_bf16 v[128:143], v[68:71], v[144:147], v[128:143]
	v_add_f32_e32 v254, v213, v254
	v_pk_add_f32 v[254:255], v[214:215], v[254:255]
	v_pk_add_f32 v[254:255], v[218:219], v[254:255]
	v_add_f32_e32 v255, v228, v255
	v_pk_add_f32 v[254:255], v[64:65], v[254:255]
	v_pk_add_f32 v[254:255], v[66:67], v[254:255]
	s_waitcnt lgkmcnt(0)
	v_mfma_f32_32x32x16_bf16 v[112:127], v[224:227], v[144:147], v[112:127]
	v_add_f32_e32 v254, v105, v254
	v_pk_add_f32 v[254:255], v[106:107], v[254:255]
	v_pk_add_f32 v[254:255], v[72:73], v[254:255]
	v_add_f32_e32 v255, v74, v255
	v_add_f32_e32 v211, v254, v255
	v_mov_b32_e32 v212, v211
	v_cvt_pk_bf16_f32 v108, v173, v175
	v_cvt_pk_bf16_f32 v109, v171, v174
	v_cvt_pk_bf16_f32 v110, v169, v172
	v_cvt_pk_bf16_f32 v111, v168, v170
	v_cvt_pk_bf16_f32 v100, v180, v182
	v_cvt_pk_bf16_f32 v101, v213, v214
	v_cvt_pk_bf16_f32 v102, v219, v228
	v_cvt_pk_bf16_f32 v103, v64, v65
	v_cvt_pk_bf16_f32 v104, v66, v67
	v_cvt_pk_bf16_f32 v105, v105, v106
	v_cvt_pk_bf16_f32 v106, v107, v72
	v_cvt_pk_bf16_f32 v107, v73, v74
	s_nop 1
	v_permlane32_swap_b32_e32 v211, v212
	v_permlane32_swap_b32_e32 v96, v98
	v_permlane32_swap_b32_e32 v97, v99
	v_permlane32_swap_b32_e32 v108, v110
	v_permlane32_swap_b32_e32 v109, v111
	v_permlane32_swap_b32_e32 v100, v102
	v_permlane32_swap_b32_e32 v101, v103
	v_permlane32_swap_b32_e32 v104, v106
	v_permlane32_swap_b32_e32 v105, v107
	s_add_u32 s66, s46, s28
	s_addc_u32 s67, s47, s29
	s_add_u32 s34, s66, 0x23808000
	s_addc_u32 s35, s67, 0
	s_add_u32 s76, s66, 0x2380a000
	s_addc_u32 s77, s67, 0
	s_add_u32 s74, s46, s24
	s_addc_u32 s75, s47, s25
	s_add_u32 s78, s74, 0x21804000
	s_addc_u32 s79, s75, 0
	v_mov_b32_e32 v64, v197
	v_mov_b32_e32 v65, v196
	global_load_dwordx4 v[176:179], v65, s[34:35]
	global_load_dwordx4 v[172:175], v65, s[76:77]
	global_load_dwordx4 v[168:171], v64, s[78:79]
	s_andn2_b64 vcc, exec, s[2:3]
	s_cbranch_vccnz .LBB4_851
	v_mov_b32_e32 v64, v188
	s_mov_b64 s[2:3], s[8:9]
	global_store_dwordx2 v64, v[184:185], s[2:3] nt

; DI void finishSM(f32x16& p0, f32x16& p1, float alpha, float& l_reg, bf16x8& pa0, bf16x8& pa1, bf16x8& pa2, bf16x8& pa3) {
; #pragma unroll
;     for (int r = 0; r < 16; ++r) p1[r] = __builtin_amdgcn_exp2f(p1[r]);
;     float ps = 0;
; #pragma unroll
;     for (int r = 0; r < 16; ++r) ps += p0[r];
; #pragma unroll
;     for (int r = 0; r < 16; ++r) ps += p1[r];
;     { auto rr = __builtin_amdgcn_permlane32_swap(__float_as_uint(ps), __float_as_uint(ps), false, false); ps = __uint_as_float(rr[0]) + __uint_as_float(rr[1]); }
;     l_reg = l_reg * alpha + ps;
;     ...
;     AT_PK4(p0, 0, pa0); AT_PK4(p0, 8, pa1); AT_PK4(p1, 0, pa2); AT_PK4(p1, 8, pa3);
;     ...
; }
; DI void qkt(f32x16& p0, f32x16& p1, const char* Ks, const bf16x8* qr, const f32x16& negm, int r32, int hi) {
; #pragma unroll
;     for (int d0 = 0; d0 < 4; ++d0) { const int cb = (d0 * 16 + hi * 8) * 2;
;         const bf16x8 b0 = *reinterpret_cast<const bf16x8*>(Ks + AT_KSWZ(r32, cb));
;         const bf16x8 b1 = *reinterpret_cast<const bf16x8*>(Ks + AT_KSWZ(32 + r32, cb));
;         p0 = __builtin_amdgcn_mfma_f32_32x32x16_bf16(b0, qr[d0], d0 == 0 ? negm : p0, 0, 0, 0);
;         p1 = __builtin_amdgcn_mfma_f32_32x32x16_bf16(b1, qr[d0], d0 == 0 ? negm : p1, 0, 0, 0); }
; }
.LBB4_870:
	v_exp_f32_e32 v182, v128
	v_exp_f32_e32 v230, v129
	v_exp_f32_e32 v231, v130
	v_exp_f32_e32 v232, v131
	v_exp_f32_e32 v233, v132
	v_exp_f32_e32 v234, v133
	v_exp_f32_e32 v235, v134
	v_exp_f32_e32 v236, v135
	v_exp_f32_e32 v237, v136
	v_exp_f32_e32 v238, v137
	v_exp_f32_e32 v239, v138
	v_exp_f32_e32 v240, v139
	v_exp_f32_e32 v241, v140
	v_exp_f32_e32 v242, v141
	v_exp_f32_e32 v243, v142
	v_exp_f32_e32 v244, v143
	v_add_u32_e32 v101, s76, v204
	v_add_u32_e32 v102, s76, v205
	v_add_u32_e32 v103, s76, v206
	ds_read_b128 v[172:175], v101 offset:49152
	ds_read_b128 v[176:179], v101 offset:53248
	ds_read_b128 v[214:217], v102 offset:49152
	ds_read_b128 v[218:221], v102 offset:53248
	ds_read_b128 v[222:225], v103 offset:49152
	ds_read_b128 v[226:229], v103 offset:53248
	v_exp_f32_e32 v112, v112
	v_exp_f32_e32 v113, v113
	v_exp_f32_e32 v114, v114
	s_waitcnt lgkmcnt(7)
	v_mfma_f32_32x32x16_bf16 v[128:143], v[96:99], v[156:159], v[80:95]
	v_exp_f32_e32 v115, v115
	v_exp_f32_e32 v116, v116
	v_exp_f32_e32 v117, v117
	v_exp_f32_e32 v118, v118
	v_exp_f32_e32 v119, v119
	s_waitcnt lgkmcnt(6)
	v_mfma_f32_32x32x16_bf16 v[96:111], v[168:171], v[156:159], v[80:95]
	v_exp_f32_e32 v168, v120
	v_mov_b32_e32 v254, v182
	v_mov_b32_e32 v255, 0
	v_pk_add_f32 v[254:255], v[230:231], v[254:255]
	v_pk_add_f32 v[254:255], v[232:233], v[254:255]
	v_pk_add_f32 v[254:255], v[234:235], v[254:255]
	v_pk_add_f32 v[254:255], v[236:237], v[254:255]
	s_waitcnt lgkmcnt(5)
	v_mfma_f32_32x32x16_bf16 v[128:143], v[172:175], v[152:155], v[128:143]
	v_pk_add_f32 v[254:255], v[238:239], v[254:255]
	v_pk_add_f32 v[254:255], v[240:241], v[254:255]
	v_pk_add_f32 v[254:255], v[242:243], v[254:255]
	v_add_f32_e32 v255, v244, v255
	s_waitcnt lgkmcnt(4)
	v_mfma_f32_32x32x16_bf16 v[96:111], v[176:179], v[152:155], v[96:111]
	v_pk_add_f32 v[254:255], v[112:113], v[254:255]
	v_pk_add_f32 v[254:255], v[114:115], v[254:255]
	v_exp_f32_e32 v169, v121
	v_pk_add_f32 v[254:255], v[116:117], v[254:255]
	v_exp_f32_e32 v170, v122
	s_waitcnt lgkmcnt(3)
	v_mfma_f32_32x32x16_bf16 v[128:143], v[214:217], v[148:151], v[128:143]
	v_exp_f32_e32 v171, v123
	v_pk_add_f32 v[254:255], v[118:119], v[254:255]
	v_exp_f32_e32 v172, v124
	v_exp_f32_e32 v173, v125
	v_pk_add_f32 v[254:255], v[168:169], v[254:255]
	s_waitcnt lgkmcnt(2)
	v_mfma_f32_32x32x16_bf16 v[96:111], v[218:221], v[148:151], v[96:111]
	v_exp_f32_e32 v174, v126
	v_exp_f32_e32 v175, v127
	v_pk_add_f32 v[254:255], v[170:171], v[254:255]
	v_pk_add_f32 v[254:255], v[172:173], v[254:255]
	s_waitcnt lgkmcnt(1)
	v_mfma_f32_32x32x16_bf16 v[128:143], v[222:225], v[144:147], v[128:143]
	v_pk_add_f32 v[254:255], v[174:175], v[254:255]
	v_add_f32_e32 v213, v254, v255
	v_mov_b32_e32 v214, v213
	v_cvt_pk_bf16_f32 v120, v182, v230
	v_cvt_pk_bf16_f32 v121, v231, v232
	v_cvt_pk_bf16_f32 v122, v233, v234
	v_cvt_pk_bf16_f32 v123, v235, v236
	v_cvt_pk_bf16_f32 v124, v237, v238
	s_waitcnt lgkmcnt(0)
	v_mfma_f32_32x32x16_bf16 v[96:111], v[226:229], v[144:147], v[96:111]
	v_cvt_pk_bf16_f32 v125, v239, v240
	v_cvt_pk_bf16_f32 v126, v241, v242
	v_cvt_pk_bf16_f32 v127, v243, v244
	v_cvt_pk_bf16_f32 v112, v112, v113
	v_cvt_pk_bf16_f32 v113, v114, v115
	v_cvt_pk_bf16_f32 v114, v116, v117
	v_cvt_pk_bf16_f32 v115, v118, v119
	v_cvt_pk_bf16_f32 v116, v168, v169
	v_cvt_pk_bf16_f32 v117, v170, v171
	v_cvt_pk_bf16_f32 v118, v172, v173
	v_cvt_pk_bf16_f32 v119, v174, v175
	v_permlane32_swap_b32_e32 v213, v214
	v_permlane32_swap_b32_e32 v120, v122
	v_permlane32_swap_b32_e32 v121, v123
	v_permlane32_swap_b32_e32 v124, v126
	v_permlane32_swap_b32_e32 v125, v127
	v_permlane32_swap_b32_e32 v112, v114
	v_permlane32_swap_b32_e32 v113, v115
	v_permlane32_swap_b32_e32 v116, v118
	v_permlane32_swap_b32_e32 v117, v119
	s_add_u32 s34, s66, 0x2380c000
	s_addc_u32 s35, s67, 0
	s_add_u32 s66, s66, 0x2380e000
	s_addc_u32 s67, s67, 0
	s_add_u32 s74, s74, 0x21806000
	s_addc_u32 s75, s75, 0
	v_mov_b32_e32 v168, v197
	v_mov_b32_e32 v169, v196
	global_load_dwordx4 v[176:179], v169, s[34:35]
	global_load_dwordx4 v[172:175], v169, s[66:67]
	s_nop 0
	global_load_dwordx4 v[168:171], v168, s[74:75]
	s_and_b64 vcc, exec, s[2:3]
	s_cbranch_vccnz .LBB4_872
	v_mov_b32_e32 v182, v188
	s_mov_b64 s[2:3], s[8:9]
	global_store_dwordx2 v182, v[184:185], s[2:3] nt

; DI void finishSM(f32x16& p0, f32x16& p1, float alpha, float& l_reg, bf16x8& pa0, bf16x8& pa1, bf16x8& pa2, bf16x8& pa3) {
; #pragma unroll
;     for (int r = 0; r < 16; ++r) p1[r] = __builtin_amdgcn_exp2f(p1[r]);
;     float ps = 0;
; #pragma unroll
;     for (int r = 0; r < 16; ++r) ps += p0[r];
; #pragma unroll
;     for (int r = 0; r < 16; ++r) ps += p1[r];
;     { auto rr = __builtin_amdgcn_permlane32_swap(__float_as_uint(ps), __float_as_uint(ps), false, false); ps = __uint_as_float(rr[0]) + __uint_as_float(rr[1]); }
;     l_reg = l_reg * alpha + ps;
;     ...
;     AT_PK4(p0, 0, pa0); AT_PK4(p0, 8, pa1); AT_PK4(p1, 0, pa2); AT_PK4(p1, 8, pa3);
;     ...
; }
; DI void qkt(f32x16& p0, f32x16& p1, const char* Ks, const bf16x8* qr, const f32x16& negm, int r32, int hi) {
; #pragma unroll
;     for (int d0 = 0; d0 < 4; ++d0) { const int cb = (d0 * 16 + hi * 8) * 2;
;         const bf16x8 b0 = *reinterpret_cast<const bf16x8*>(Ks + AT_KSWZ(r32, cb));
;         const bf16x8 b1 = *reinterpret_cast<const bf16x8*>(Ks + AT_KSWZ(32 + r32, cb));
;         p0 = __builtin_amdgcn_mfma_f32_32x32x16_bf16(b0, qr[d0], d0 == 0 ? negm : p0, 0, 0, 0);
;         p1 = __builtin_amdgcn_mfma_f32_32x32x16_bf16(b1, qr[d0], d0 == 0 ? negm : p1, 0, 0, 0); }
; }
.LBB4_923:
	s_lshl_b32 s18, s30, 13
	s_add_i32 s18, s18, 0
	v_add_u32_e32 v72, s18, v208
	v_add_u32_e32 v112, s18, v209
	v_add_u32_e32 v180, s18, v210
	s_waitcnt lgkmcnt(1)
	v_mfma_f32_32x32x16_bf16 v[128:143], v[64:67], v[156:159], v[80:95]
	ds_read_b128 v[64:67], v72 offset:49152
	ds_read_b128 v[72:75], v72 offset:53248
	ds_read_b128 v[76:79], v112 offset:49152
	ds_read_b128 v[224:227], v112 offset:53248
	v_exp_f32_e32 v182, v97
	v_exp_f32_e32 v217, v98
	v_exp_f32_e32 v218, v99
	v_exp_f32_e32 v223, v100
	v_exp_f32_e32 v232, v101
	s_waitcnt lgkmcnt(4)
	v_mfma_f32_32x32x16_bf16 v[112:127], v[68:71], v[156:159], v[80:95]
	ds_read_b128 v[68:71], v180 offset:49152
	ds_read_b128 v[228:231], v180 offset:53248
	v_exp_f32_e32 v180, v96
	v_cvt_pk_bf16_f32 v96, v220, v222
	v_cvt_pk_bf16_f32 v97, v179, v221
	v_cvt_pk_bf16_f32 v98, v177, v219
	v_cvt_pk_bf16_f32 v99, v176, v178
	s_waitcnt lgkmcnt(4)
	v_mfma_f32_32x32x16_bf16 v[112:127], v[72:75], v[152:155], v[112:127]
	v_pk_add_f32 v[254:255], v[220:221], 0 op_sel_hi:[1,0]
	v_pk_add_f32 v[254:255], v[176:177], v[254:255]
	v_mfma_f32_32x32x16_bf16 v[128:143], v[64:67], v[152:155], v[128:143]
	v_pk_add_f32 v[254:255], v[178:179], v[254:255]
	v_pk_add_f32 v[254:255], v[174:175], v[254:255]
	v_pk_add_f32 v[254:255], v[172:173], v[254:255]
	s_waitcnt lgkmcnt(3)
	v_mfma_f32_32x32x16_bf16 v[128:143], v[76:79], v[148:151], v[128:143]
	v_pk_add_f32 v[254:255], v[168:169], v[254:255]
	v_pk_add_f32 v[254:255], v[170:171], v[254:255]
	v_add_f32_e32 v254, v180, v254
	v_add_f32_e32 v255, v182, v255
	v_exp_f32_e32 v64, v102
	v_exp_f32_e32 v65, v103
	v_exp_f32_e32 v66, v104
	s_waitcnt lgkmcnt(2)
	v_mfma_f32_32x32x16_bf16 v[112:127], v[224:227], v[148:151], v[112:127]
	v_exp_f32_e32 v67, v105
	v_exp_f32_e32 v105, v106
	v_exp_f32_e32 v106, v107
	v_exp_f32_e32 v107, v108
	v_exp_f32_e32 v72, v109
	v_exp_f32_e32 v73, v110
	v_exp_f32_e32 v74, v111
	s_waitcnt lgkmcnt(1)
	v_mfma_f32_32x32x16_bf16 v[128:143], v[68:71], v[144:147], v[128:143]
	v_add_f32_e32 v254, v217, v254
	v_pk_add_f32 v[254:255], v[218:219], v[254:255]
	v_pk_add_f32 v[254:255], v[222:223], v[254:255]
	v_add_f32_e32 v255, v232, v255
	v_pk_add_f32 v[254:255], v[64:65], v[254:255]
	v_pk_add_f32 v[254:255], v[66:67], v[254:255]
	s_waitcnt lgkmcnt(0)
	v_mfma_f32_32x32x16_bf16 v[112:127], v[228:231], v[144:147], v[112:127]
	v_add_f32_e32 v254, v105, v254
	v_pk_add_f32 v[254:255], v[106:107], v[254:255]
	v_pk_add_f32 v[254:255], v[72:73], v[254:255]
	v_add_f32_e32 v255, v74, v255
	v_add_f32_e32 v215, v254, v255
	v_mov_b32_e32 v216, v215
	v_cvt_pk_bf16_f32 v108, v173, v175
	v_cvt_pk_bf16_f32 v109, v171, v174
	v_cvt_pk_bf16_f32 v110, v169, v172
	v_cvt_pk_bf16_f32 v111, v168, v170
	v_cvt_pk_bf16_f32 v100, v180, v182
	v_cvt_pk_bf16_f32 v101, v217, v218
	v_cvt_pk_bf16_f32 v102, v223, v232
	v_cvt_pk_bf16_f32 v103, v64, v65
	v_cvt_pk_bf16_f32 v104, v66, v67
	v_cvt_pk_bf16_f32 v105, v105, v106
	v_cvt_pk_bf16_f32 v106, v107, v72
	v_cvt_pk_bf16_f32 v107, v73, v74
	s_nop 1
	v_permlane32_swap_b32_e32 v215, v216
	v_permlane32_swap_b32_e32 v96, v98
	v_permlane32_swap_b32_e32 v97, v99
	v_permlane32_swap_b32_e32 v108, v110
	v_permlane32_swap_b32_e32 v109, v111
	v_permlane32_swap_b32_e32 v100, v102
	v_permlane32_swap_b32_e32 v101, v103
	v_permlane32_swap_b32_e32 v104, v106
	v_permlane32_swap_b32_e32 v105, v107
	s_add_u32 s34, s46, s16
	s_addc_u32 s35, s47, s17
	s_add_u32 s24, s34, 0x23808000
	s_addc_u32 s25, s35, 0
	s_add_u32 s54, s34, 0x2380a000
	s_addc_u32 s55, s35, 0
	s_add_u32 s42, s46, s20
	s_addc_u32 s43, s47, s21
	s_add_u32 s56, s42, 0x21884000
	s_addc_u32 s57, s43, 0
	v_mov_b32_e32 v64, v201
	v_mov_b32_e32 v65, v200
	global_load_dwordx4 v[176:179], v65, s[24:25]
	global_load_dwordx4 v[172:175], v65, s[54:55]
	global_load_dwordx4 v[168:171], v64, s[56:57]
	s_andn2_b64 vcc, exec, s[2:3]
	s_cbranch_vccnz .LBB4_925
	v_mov_b32_e32 v64, v193
	s_mov_b64 s[2:3], s[8:9]
	global_store_dwordx2 v64, v[184:185], s[2:3] nt

; DI void finishSM(f32x16& p0, f32x16& p1, float alpha, float& l_reg, bf16x8& pa0, bf16x8& pa1, bf16x8& pa2, bf16x8& pa3) {
; #pragma unroll
;     for (int r = 0; r < 16; ++r) p1[r] = __builtin_amdgcn_exp2f(p1[r]);
;     float ps = 0;
; #pragma unroll
;     for (int r = 0; r < 16; ++r) ps += p0[r];
; #pragma unroll
;     for (int r = 0; r < 16; ++r) ps += p1[r];
;     { auto rr = __builtin_amdgcn_permlane32_swap(__float_as_uint(ps), __float_as_uint(ps), false, false); ps = __uint_as_float(rr[0]) + __uint_as_float(rr[1]); }
;     l_reg = l_reg * alpha + ps;
;     ...
;     AT_PK4(p0, 0, pa0); AT_PK4(p0, 8, pa1); AT_PK4(p1, 0, pa2); AT_PK4(p1, 8, pa3);
;     ...
; }
; DI void qkt(f32x16& p0, f32x16& p1, const char* Ks, const bf16x8* qr, const f32x16& negm, int r32, int hi) {
; #pragma unroll
;     for (int d0 = 0; d0 < 4; ++d0) { const int cb = (d0 * 16 + hi * 8) * 2;
;         const bf16x8 b0 = *reinterpret_cast<const bf16x8*>(Ks + AT_KSWZ(r32, cb));
;         const bf16x8 b1 = *reinterpret_cast<const bf16x8*>(Ks + AT_KSWZ(32 + r32, cb));
;         p0 = __builtin_amdgcn_mfma_f32_32x32x16_bf16(b0, qr[d0], d0 == 0 ? negm : p0, 0, 0, 0);
;         p1 = __builtin_amdgcn_mfma_f32_32x32x16_bf16(b1, qr[d0], d0 == 0 ? negm : p1, 0, 0, 0); }
.LBB4_944:
	v_exp_f32_e32 v182, v128
	v_exp_f32_e32 v234, v129
	v_exp_f32_e32 v235, v130
	v_exp_f32_e32 v236, v131
	v_exp_f32_e32 v237, v132
	v_exp_f32_e32 v238, v133
	v_exp_f32_e32 v239, v134
	v_exp_f32_e32 v240, v135
	v_exp_f32_e32 v241, v136
	v_exp_f32_e32 v242, v137
	v_exp_f32_e32 v243, v138
	v_exp_f32_e32 v244, v139
	v_exp_f32_e32 v245, v140
	v_exp_f32_e32 v246, v141
	v_exp_f32_e32 v247, v142
	v_exp_f32_e32 v248, v143
	v_add_u32_e32 v101, s54, v208
	v_add_u32_e32 v102, s54, v209
	v_add_u32_e32 v103, s54, v210
	ds_read_b128 v[172:175], v101 offset:49152
	ds_read_b128 v[176:179], v101 offset:53248
	ds_read_b128 v[218:221], v102 offset:49152
	ds_read_b128 v[222:225], v102 offset:53248
	ds_read_b128 v[226:229], v103 offset:49152
	ds_read_b128 v[230:233], v103 offset:53248
	v_exp_f32_e32 v112, v112
	v_exp_f32_e32 v113, v113
	v_exp_f32_e32 v114, v114
	s_waitcnt lgkmcnt(7)
	v_mfma_f32_32x32x16_bf16 v[128:143], v[96:99], v[156:159], v[80:95]
	v_exp_f32_e32 v115, v115
	v_exp_f32_e32 v116, v116
	v_exp_f32_e32 v117, v117
	v_exp_f32_e32 v118, v118
	v_exp_f32_e32 v119, v119
	s_waitcnt lgkmcnt(6)
	v_mfma_f32_32x32x16_bf16 v[96:111], v[168:171], v[156:159], v[80:95]
	v_exp_f32_e32 v168, v120
	v_mov_b32_e32 v254, v182
	v_mov_b32_e32 v255, 0
	v_pk_add_f32 v[254:255], v[234:235], v[254:255]
	v_pk_add_f32 v[254:255], v[236:237], v[254:255]
	v_pk_add_f32 v[254:255], v[238:239], v[254:255]
	v_pk_add_f32 v[254:255], v[240:241], v[254:255]
	s_waitcnt lgkmcnt(5)
	v_mfma_f32_32x32x16_bf16 v[128:143], v[172:175], v[152:155], v[128:143]
	v_pk_add_f32 v[254:255], v[242:243], v[254:255]
	v_pk_add_f32 v[254:255], v[244:245], v[254:255]
	v_pk_add_f32 v[254:255], v[246:247], v[254:255]
	v_add_f32_e32 v255, v248, v255
	s_waitcnt lgkmcnt(4)
	v_mfma_f32_32x32x16_bf16 v[96:111], v[176:179], v[152:155], v[96:111]
	v_pk_add_f32 v[254:255], v[112:113], v[254:255]
	v_pk_add_f32 v[254:255], v[114:115], v[254:255]
	v_exp_f32_e32 v169, v121
	v_pk_add_f32 v[254:255], v[116:117], v[254:255]
	v_exp_f32_e32 v170, v122
	s_waitcnt lgkmcnt(3)
	v_mfma_f32_32x32x16_bf16 v[128:143], v[218:221], v[148:151], v[128:143]
	v_exp_f32_e32 v171, v123
	v_pk_add_f32 v[254:255], v[118:119], v[254:255]
	v_exp_f32_e32 v172, v124
	v_exp_f32_e32 v173, v125
	v_pk_add_f32 v[254:255], v[168:169], v[254:255]
	s_waitcnt lgkmcnt(2)
	v_mfma_f32_32x32x16_bf16 v[96:111], v[222:225], v[148:151], v[96:111]
	v_exp_f32_e32 v174, v126
	v_exp_f32_e32 v175, v127
	v_pk_add_f32 v[254:255], v[170:171], v[254:255]
	v_pk_add_f32 v[254:255], v[172:173], v[254:255]
	s_waitcnt lgkmcnt(1)
	v_mfma_f32_32x32x16_bf16 v[128:143], v[226:229], v[144:147], v[128:143]
	v_pk_add_f32 v[254:255], v[174:175], v[254:255]
	v_add_f32_e32 v217, v254, v255
	v_mov_b32_e32 v218, v217
	v_cvt_pk_bf16_f32 v120, v182, v234
	v_cvt_pk_bf16_f32 v121, v235, v236
	v_cvt_pk_bf16_f32 v122, v237, v238
	v_cvt_pk_bf16_f32 v123, v239, v240
	v_cvt_pk_bf16_f32 v124, v241, v242
	s_waitcnt lgkmcnt(0)
	v_mfma_f32_32x32x16_bf16 v[96:111], v[230:233], v[144:147], v[96:111]
	v_cvt_pk_bf16_f32 v125, v243, v244
	v_cvt_pk_bf16_f32 v126, v245, v246
	v_cvt_pk_bf16_f32 v127, v247, v248
	v_cvt_pk_bf16_f32 v112, v112, v113
	v_cvt_pk_bf16_f32 v113, v114, v115
	v_cvt_pk_bf16_f32 v114, v116, v117
	v_cvt_pk_bf16_f32 v115, v118, v119
	v_cvt_pk_bf16_f32 v116, v168, v169
	v_cvt_pk_bf16_f32 v117, v170, v171
	v_cvt_pk_bf16_f32 v118, v172, v173
	v_cvt_pk_bf16_f32 v119, v174, v175
	v_permlane32_swap_b32_e32 v217, v218
	v_permlane32_swap_b32_e32 v120, v122
	v_permlane32_swap_b32_e32 v121, v123
	v_permlane32_swap_b32_e32 v124, v126
	v_permlane32_swap_b32_e32 v125, v127
	v_permlane32_swap_b32_e32 v112, v114
	v_permlane32_swap_b32_e32 v113, v115
	v_permlane32_swap_b32_e32 v116, v118
	v_permlane32_swap_b32_e32 v117, v119
	s_add_u32 s24, s34, 0x2380c000
	s_addc_u32 s25, s35, 0
	s_add_u32 s34, s34, 0x2380e000
	s_addc_u32 s35, s35, 0
	s_add_u32 s42, s42, 0x21886000
	s_addc_u32 s43, s43, 0
	v_mov_b32_e32 v168, v201
	v_mov_b32_e32 v169, v200
	global_load_dwordx4 v[176:179], v169, s[24:25]
	global_load_dwordx4 v[172:175], v169, s[34:35]
	s_nop 0
	global_load_dwordx4 v[168:171], v168, s[42:43]
	s_and_b64 vcc, exec, s[2:3]
	s_cbranch_vccnz .LBB4_946
	s_mov_b64 s[2:3], s[8:9]
	v_mov_b32_e32 v182, v193
	global_store_dwordx2 v182, v[184:185], s[2:3] nt
